# agg1: nodes of a block ranked by degree (bitonic sort), each wave takes 8 nodes of similar degree
# speedup vs baseline: 1.0078x; 1.0078x over previous
_Z11agg1_kernelPKDF16_PKfS2_PKiS4_S2_S2_PDF16_PfS6_i:
	s_load_dwordx8 s[4:11], s[0:1], 0x0
	s_load_dwordx8 s[12:19], s[0:1], 0x20
	s_load_dwordx4 s[20:23], s[0:1], 0x40
	s_load_dword s24, s[0:1], 0x50
	v_lshlrev_b32_e32 v32, 2, v0
	v_readfirstlane_b32 s25, v0
	s_lshl_b32 s26, s2, 5
	v_and_b32_e32 v64, 7, v0
	v_bfe_u32 v65, v0, 3, 3
	v_and_b32_e32 v45, 31, v0
	s_lshr_b32 s25, s25, 6
	v_lshlrev_b32_e32 v1, 1, v64
	v_add_u32_e32 v46, s26, v45
	s_waitcnt lgkmcnt(0)
	global_load_dword v33, v32, s[14:15]
	global_load_dword v34, v32, s[16:17]
	s_add_i32 s28, s24, -1
	v_cmp_gt_i32_e64 s[38:39], s24, v46
	v_min_i32_e32 v46, s28, v46
	v_lshlrev_b32_e32 v47, 2, v46
	global_load_dword v44, v47, s[10:11]
	global_load_dword v48, v47, s[10:11] offset:4
	s_lshl_b32 s27, s25, 11
	v_lshlrev_b32_e32 v62, 6, v64
	v_add_u32_e32 v62, 0x2000, v62
	v_cmp_eq_u32_e64 s[34:35], 0, v64
	v_lshlrev_b32_e32 v35, 8, v64
	v_lshl_add_u32 v35, v65, 4, v35
	v_add_u32_e32 v63, s27, v35
	v_mov_b32_e32 v36, 0
	v_mov_b32_e32 v37, 0
	v_mov_b32_e32 v38, 0
	v_mov_b32_e32 v39, 0
	s_waitcnt vmcnt(2)
	ds_write2st64_b32 v32, v33, v34 offset0:32 offset1:36
	ds_write_b128 v63, v[36:39]
	ds_write_b128 v63, v[36:39] offset:128
	s_waitcnt vmcnt(0)
	v_sub_u32_e32 v48, v48, v44
	v_add_u32_e32 v48, 1, v48
	v_cndmask_b32_e64 v48, 0, v48, s[38:39]
	v_lshl_or_b32 v40, v48, 5, v45
	s_nop 1
	v_mov_b32_dpp v41, v40 quad_perm:[1,0,3,2] row_mask:0xf bank_mask:0xf
	s_mov_b32 s40, 0x99999999
	s_mov_b32 s41, 0x99999999
	v_min_u32_e32 v42, v40, v41
	v_max_u32_e32 v43, v40, v41
	v_cndmask_b32_e64 v40, v42, v43, s[40:41]
	s_nop 1
	v_mov_b32_dpp v41, v40 quad_perm:[2,3,0,1] row_mask:0xf bank_mask:0xf
	s_mov_b32 s40, 0xc3c3c3c3
	s_mov_b32 s41, 0xc3c3c3c3
	v_min_u32_e32 v42, v40, v41
	v_max_u32_e32 v43, v40, v41
	v_cndmask_b32_e64 v40, v42, v43, s[40:41]
	s_nop 1
	v_mov_b32_dpp v41, v40 quad_perm:[1,0,3,2] row_mask:0xf bank_mask:0xf
	s_mov_b32 s40, 0xa5a5a5a5
	s_mov_b32 s41, 0xa5a5a5a5
	v_min_u32_e32 v42, v40, v41
	v_max_u32_e32 v43, v40, v41
	v_cndmask_b32_e64 v40, v42, v43, s[40:41]
	ds_swizzle_b32 v41, v40 offset:swizzle(SWAP,4)
	s_waitcnt lgkmcnt(0)
	s_mov_b32 s40, 0xf00ff00f
	s_mov_b32 s41, 0xf00ff00f
	v_min_u32_e32 v42, v40, v41
	v_max_u32_e32 v43, v40, v41
	v_cndmask_b32_e64 v40, v42, v43, s[40:41]
	s_nop 1
	v_mov_b32_dpp v41, v40 quad_perm:[2,3,0,1] row_mask:0xf bank_mask:0xf
	s_mov_b32 s40, 0xcc33cc33
	s_mov_b32 s41, 0xcc33cc33
	v_min_u32_e32 v42, v40, v41
	v_max_u32_e32 v43, v40, v41
	v_cndmask_b32_e64 v40, v42, v43, s[40:41]
	s_nop 1
	v_mov_b32_dpp v41, v40 quad_perm:[1,0,3,2] row_mask:0xf bank_mask:0xf
	s_mov_b32 s40, 0xaa55aa55
	s_mov_b32 s41, 0xaa55aa55
	v_min_u32_e32 v42, v40, v41
	v_max_u32_e32 v43, v40, v41
	v_cndmask_b32_e64 v40, v42, v43, s[40:41]
	ds_swizzle_b32 v41, v40 offset:swizzle(SWAP,8)
	s_waitcnt lgkmcnt(0)
	s_mov_b32 s40, 0xff0000ff
	s_mov_b32 s41, 0xff0000ff
	v_min_u32_e32 v42, v40, v41
	v_max_u32_e32 v43, v40, v41
	v_cndmask_b32_e64 v40, v42, v43, s[40:41]
	ds_swizzle_b32 v41, v40 offset:swizzle(SWAP,4)
	s_waitcnt lgkmcnt(0)
	s_mov_b32 s40, 0xf0f00f0f
	s_mov_b32 s41, 0xf0f00f0f
	v_min_u32_e32 v42, v40, v41
	v_max_u32_e32 v43, v40, v41
	v_cndmask_b32_e64 v40, v42, v43, s[40:41]
	s_nop 1
	v_mov_b32_dpp v41, v40 quad_perm:[2,3,0,1] row_mask:0xf bank_mask:0xf
	s_mov_b32 s40, 0xcccc3333
	s_mov_b32 s41, 0xcccc3333
	v_min_u32_e32 v42, v40, v41
	v_max_u32_e32 v43, v40, v41
	v_cndmask_b32_e64 v40, v42, v43, s[40:41]
	s_nop 1
	v_mov_b32_dpp v41, v40 quad_perm:[1,0,3,2] row_mask:0xf bank_mask:0xf
	s_mov_b32 s40, 0xaaaa5555
	s_mov_b32 s41, 0xaaaa5555
	v_min_u32_e32 v42, v40, v41
	v_max_u32_e32 v43, v40, v41
	v_cndmask_b32_e64 v40, v42, v43, s[40:41]
	ds_swizzle_b32 v41, v40 offset:swizzle(SWAP,16)
	s_waitcnt lgkmcnt(0)
	s_mov_b32 s40, 0xffff
	s_mov_b32 s41, 0xffff
	v_min_u32_e32 v42, v40, v41
	v_max_u32_e32 v43, v40, v41
	v_cndmask_b32_e64 v40, v42, v43, s[40:41]
	ds_swizzle_b32 v41, v40 offset:swizzle(SWAP,8)
	s_waitcnt lgkmcnt(0)
	s_mov_b32 s40, 0xff00ff
	s_mov_b32 s41, 0xff00ff
	v_min_u32_e32 v42, v40, v41
	v_max_u32_e32 v43, v40, v41
	v_cndmask_b32_e64 v40, v42, v43, s[40:41]
	ds_swizzle_b32 v41, v40 offset:swizzle(SWAP,4)
	s_waitcnt lgkmcnt(0)
	s_mov_b32 s40, 0xf0f0f0f
	s_mov_b32 s41, 0xf0f0f0f
	v_min_u32_e32 v42, v40, v41
	v_max_u32_e32 v43, v40, v41
	v_cndmask_b32_e64 v40, v42, v43, s[40:41]
	s_nop 1
	v_mov_b32_dpp v41, v40 quad_perm:[2,3,0,1] row_mask:0xf bank_mask:0xf
	s_mov_b32 s40, 0x33333333
	s_mov_b32 s41, 0x33333333
	v_min_u32_e32 v42, v40, v41
	v_max_u32_e32 v43, v40, v41
	v_cndmask_b32_e64 v40, v42, v43, s[40:41]
	s_nop 1
	v_mov_b32_dpp v41, v40 quad_perm:[1,0,3,2] row_mask:0xf bank_mask:0xf
	s_mov_b32 s40, 0x55555555
	s_mov_b32 s41, 0x55555555
	v_min_u32_e32 v42, v40, v41
	v_max_u32_e32 v43, v40, v41
	v_cndmask_b32_e64 v40, v42, v43, s[40:41]
	s_lshl_b32 s40, s25, 3
	v_add_u32_e32 v45, s40, v65
	v_lshlrev_b32_e32 v45, 2, v45
	ds_bpermute_b32 v46, v45, v40
	s_waitcnt lgkmcnt(0)
	v_and_b32_e32 v15, 31, v46
	v_lshrrev_b32_e32 v11, 5, v46
	v_lshlrev_b32_e32 v47, 2, v15
	ds_bpermute_b32 v10, v47, v44
	v_add_u32_e32 v66, s26, v15
	v_min_i32_e32 v66, s28, v66
	v_cmp_lt_u32_e64 s[36:37], 0, v11
	v_lshlrev_b32_e32 v4, 2, v66
	v_lshlrev_b32_e32 v35, 2, v64
	v_lshl_or_b32 v35, v66, 5, v35
	global_load_dword v9, v35, s[8:9]
	v_lshrrev_b32_e32 v3, 3, v15
	v_lshlrev_b32_e32 v3, 11, v3
	v_and_b32_e32 v47, 7, v15
	v_lshl_add_u32 v3, v47, 1, v3
	v_lshl_add_u32 v3, v64, 4, v3
	v_readfirstlane_b32 s29, v11
	s_waitcnt lgkmcnt(0)
	s_barrier
	v_add_u32_e32 v67, v10, v64
	v_lshlrev_b32_e32 v67, 2, v67
	v_mov_b32_e32 v5, s24
	v_mov_b32_e32 v6, s24
	v_mov_b32_e32 v7, s24
	v_mov_b32_e32 v8, s24
	v_cndmask_b32_e64 v5, v5, v66, s[34:35]
	v_cmp_gt_i32_e32 vcc, v11, v64
	s_andn2_b64 s[40:41], vcc, s[34:35]
	s_and_saveexec_b64 s[32:33], s[40:41]
	global_load_dword v5, v67, s[12:13] offset:-4
	s_mov_b64 exec, s[32:33]
	v_add_u32_e32 v68, 8, v64
	v_cmp_gt_i32_e32 vcc, v11, v68
	s_and_saveexec_b64 s[32:33], vcc
	global_load_dword v6, v67, s[12:13] offset:28
	s_mov_b64 exec, s[32:33]
	v_add_u32_e32 v68, 16, v64
	v_cmp_gt_i32_e32 vcc, v11, v68
	s_and_saveexec_b64 s[32:33], vcc
	global_load_dword v7, v67, s[12:13] offset:60
	s_mov_b64 exec, s[32:33]
	v_add_u32_e32 v68, 24, v64
	v_cmp_gt_i32_e32 vcc, v11, v68
	s_and_saveexec_b64 s[32:33], vcc
	global_load_dword v8, v67, s[12:13] offset:92
	s_mov_b64 exec, s[32:33]
	s_waitcnt vmcnt(0)
	v_lshlrev_b32_e32 v5, 4, v5
	v_lshlrev_b32_e32 v6, 4, v6
	v_lshlrev_b32_e32 v7, 4, v7
	v_lshlrev_b32_e32 v8, 4, v8
	s_mov_b32 s42, 0
	s_mov_b32 s43, 0
	s_cmp_lt_i32 s29, 3
	s_cbranch_scc1 .Lagg_first_half
	ds_swizzle_b32 v32, v5 offset:swizzle(BITMASK_PERM, "pp000")
	ds_swizzle_b32 v33, v5 offset:swizzle(BITMASK_PERM, "pp001")
	ds_swizzle_b32 v34, v5 offset:swizzle(BITMASK_PERM, "pp010")
	ds_swizzle_b32 v35, v5 offset:swizzle(BITMASK_PERM, "pp011")
	s_waitcnt lgkmcnt(0)
	v_or_b32_e32 v32, v32, v1
	v_or_b32_e32 v33, v33, v1
	v_or_b32_e32 v34, v34, v1
	v_or_b32_e32 v35, v35, v1
	global_load_ushort v36, v32, s[6:7]
	global_load_ushort v37, v33, s[6:7]
	global_load_ushort v38, v34, s[6:7]
	global_load_ushort v39, v35, s[6:7]
	v_lshlrev_b32_e32 v32, 3, v32
	v_lshlrev_b32_e32 v33, 3, v33
	v_lshlrev_b32_e32 v34, 3, v34
	v_lshlrev_b32_e32 v35, 3, v35
	global_load_dwordx4 v[40:43], v32, s[4:5]
	global_load_dwordx4 v[44:47], v33, s[4:5]
	global_load_dwordx4 v[48:51], v34, s[4:5]
	global_load_dwordx4 v[52:55], v35, s[4:5]
	s_waitcnt vmcnt(4)
	v_fma_mix_f32 v36, v36, 1.0, v9 op_sel_hi:[1,0,0]
	v_fma_mix_f32 v37, v37, 1.0, v9 op_sel_hi:[1,0,0]
	v_fma_mix_f32 v38, v38, 1.0, v9 op_sel_hi:[1,0,0]
	v_fma_mix_f32 v39, v39, 1.0, v9 op_sel_hi:[1,0,0]
	v_mul_f32_e32 v58, 0x3e4ccccd, v36
	v_mul_f32_e32 v59, 0x3e4ccccd, v37
	v_mul_f32_e32 v60, 0x3e4ccccd, v38
	v_mul_f32_e32 v61, 0x3e4ccccd, v39
	v_max_f32_e32 v36, v36, v58
	v_max_f32_e32 v37, v37, v59
	v_max_f32_e32 v38, v38, v60
	v_max_f32_e32 v39, v39, v61
	v_max3_f32 v56, v36, v37, v38
	v_max_f32_e32 v13, v56, v39
	v_sub_f32_e32 v36, v36, v13
	v_sub_f32_e32 v37, v37, v13
	v_sub_f32_e32 v38, v38, v13
	v_sub_f32_e32 v39, v39, v13
	v_exp_f32_e32 v36, v36
	v_exp_f32_e32 v37, v37
	v_exp_f32_e32 v38, v38
	v_exp_f32_e32 v39, v39
	s_nop 0
	v_add_f32_e32 v14, v36, v37
	v_add_f32_e32 v14, v14, v38
	v_add_f32_e32 v14, v14, v39
	s_waitcnt vmcnt(3)
	v_cvt_scalef32_pk_f16_fp8 v58, v40, 1.0
	v_cvt_scalef32_pk_f16_fp8 v59, v40, 1.0 op_sel:[1,0,0]
	v_cvt_scalef32_pk_f16_fp8 v60, v41, 1.0
	v_cvt_scalef32_pk_f16_fp8 v61, v41, 1.0 op_sel:[1,0,0]
	v_fma_mix_f32 v16, v58, v36, 0 op_sel_hi:[1,0,0]
	v_fma_mix_f32 v17, v58, v36, 0 op_sel:[1,0,0] op_sel_hi:[1,0,0]
	v_fma_mix_f32 v18, v59, v36, 0 op_sel_hi:[1,0,0]
	v_fma_mix_f32 v19, v59, v36, 0 op_sel:[1,0,0] op_sel_hi:[1,0,0]
	v_fma_mix_f32 v20, v60, v36, 0 op_sel_hi:[1,0,0]
	v_fma_mix_f32 v21, v60, v36, 0 op_sel:[1,0,0] op_sel_hi:[1,0,0]
	v_fma_mix_f32 v22, v61, v36, 0 op_sel_hi:[1,0,0]
	v_fma_mix_f32 v23, v61, v36, 0 op_sel:[1,0,0] op_sel_hi:[1,0,0]
	v_cvt_scalef32_pk_f16_fp8 v58, v42, 1.0
	v_cvt_scalef32_pk_f16_fp8 v59, v42, 1.0 op_sel:[1,0,0]
	v_cvt_scalef32_pk_f16_fp8 v60, v43, 1.0
	v_cvt_scalef32_pk_f16_fp8 v61, v43, 1.0 op_sel:[1,0,0]
	v_fma_mix_f32 v24, v58, v36, 0 op_sel_hi:[1,0,0]
	v_fma_mix_f32 v25, v58, v36, 0 op_sel:[1,0,0] op_sel_hi:[1,0,0]
	v_fma_mix_f32 v26, v59, v36, 0 op_sel_hi:[1,0,0]
	v_fma_mix_f32 v27, v59, v36, 0 op_sel:[1,0,0] op_sel_hi:[1,0,0]
	v_fma_mix_f32 v28, v60, v36, 0 op_sel_hi:[1,0,0]
	v_fma_mix_f32 v29, v60, v36, 0 op_sel:[1,0,0] op_sel_hi:[1,0,0]
	v_fma_mix_f32 v30, v61, v36, 0 op_sel_hi:[1,0,0]
	v_fma_mix_f32 v31, v61, v36, 0 op_sel:[1,0,0] op_sel_hi:[1,0,0]
	s_waitcnt vmcnt(2)
	v_cvt_scalef32_pk_f16_fp8 v58, v44, 1.0
	v_cvt_scalef32_pk_f16_fp8 v59, v44, 1.0 op_sel:[1,0,0]
	v_cvt_scalef32_pk_f16_fp8 v60, v45, 1.0
	v_cvt_scalef32_pk_f16_fp8 v61, v45, 1.0 op_sel:[1,0,0]
	v_fma_mix_f32 v16, v58, v37, v16 op_sel_hi:[1,0,0]
	v_fma_mix_f32 v17, v58, v37, v17 op_sel:[1,0,0] op_sel_hi:[1,0,0]
	v_fma_mix_f32 v18, v59, v37, v18 op_sel_hi:[1,0,0]
	v_fma_mix_f32 v19, v59, v37, v19 op_sel:[1,0,0] op_sel_hi:[1,0,0]
	v_fma_mix_f32 v20, v60, v37, v20 op_sel_hi:[1,0,0]
	v_fma_mix_f32 v21, v60, v37, v21 op_sel:[1,0,0] op_sel_hi:[1,0,0]
	v_fma_mix_f32 v22, v61, v37, v22 op_sel_hi:[1,0,0]
	v_fma_mix_f32 v23, v61, v37, v23 op_sel:[1,0,0] op_sel_hi:[1,0,0]
	v_cvt_scalef32_pk_f16_fp8 v58, v46, 1.0
	v_cvt_scalef32_pk_f16_fp8 v59, v46, 1.0 op_sel:[1,0,0]
	v_cvt_scalef32_pk_f16_fp8 v60, v47, 1.0
	v_cvt_scalef32_pk_f16_fp8 v61, v47, 1.0 op_sel:[1,0,0]
	v_fma_mix_f32 v24, v58, v37, v24 op_sel_hi:[1,0,0]
	v_fma_mix_f32 v25, v58, v37, v25 op_sel:[1,0,0] op_sel_hi:[1,0,0]
	v_fma_mix_f32 v26, v59, v37, v26 op_sel_hi:[1,0,0]
	v_fma_mix_f32 v27, v59, v37, v27 op_sel:[1,0,0] op_sel_hi:[1,0,0]
	v_fma_mix_f32 v28, v60, v37, v28 op_sel_hi:[1,0,0]
	v_fma_mix_f32 v29, v60, v37, v29 op_sel:[1,0,0] op_sel_hi:[1,0,0]
	v_fma_mix_f32 v30, v61, v37, v30 op_sel_hi:[1,0,0]
	v_fma_mix_f32 v31, v61, v37, v31 op_sel:[1,0,0] op_sel_hi:[1,0,0]
	s_waitcnt vmcnt(1)
	v_cvt_scalef32_pk_f16_fp8 v58, v48, 1.0
	v_cvt_scalef32_pk_f16_fp8 v59, v48, 1.0 op_sel:[1,0,0]
	v_cvt_scalef32_pk_f16_fp8 v60, v49, 1.0
	v_cvt_scalef32_pk_f16_fp8 v61, v49, 1.0 op_sel:[1,0,0]
	v_fma_mix_f32 v16, v58, v38, v16 op_sel_hi:[1,0,0]
	v_fma_mix_f32 v17, v58, v38, v17 op_sel:[1,0,0] op_sel_hi:[1,0,0]
	v_fma_mix_f32 v18, v59, v38, v18 op_sel_hi:[1,0,0]
	v_fma_mix_f32 v19, v59, v38, v19 op_sel:[1,0,0] op_sel_hi:[1,0,0]
	v_fma_mix_f32 v20, v60, v38, v20 op_sel_hi:[1,0,0]
	v_fma_mix_f32 v21, v60, v38, v21 op_sel:[1,0,0] op_sel_hi:[1,0,0]
	v_fma_mix_f32 v22, v61, v38, v22 op_sel_hi:[1,0,0]
	v_fma_mix_f32 v23, v61, v38, v23 op_sel:[1,0,0] op_sel_hi:[1,0,0]
	v_cvt_scalef32_pk_f16_fp8 v58, v50, 1.0
	v_cvt_scalef32_pk_f16_fp8 v59, v50, 1.0 op_sel:[1,0,0]
	v_cvt_scalef32_pk_f16_fp8 v60, v51, 1.0
	v_cvt_scalef32_pk_f16_fp8 v61, v51, 1.0 op_sel:[1,0,0]
	v_fma_mix_f32 v24, v58, v38, v24 op_sel_hi:[1,0,0]
	v_fma_mix_f32 v25, v58, v38, v25 op_sel:[1,0,0] op_sel_hi:[1,0,0]
	v_fma_mix_f32 v26, v59, v38, v26 op_sel_hi:[1,0,0]
	v_fma_mix_f32 v27, v59, v38, v27 op_sel:[1,0,0] op_sel_hi:[1,0,0]
	v_fma_mix_f32 v28, v60, v38, v28 op_sel_hi:[1,0,0]
	v_fma_mix_f32 v29, v60, v38, v29 op_sel:[1,0,0] op_sel_hi:[1,0,0]
	v_fma_mix_f32 v30, v61, v38, v30 op_sel_hi:[1,0,0]
	v_fma_mix_f32 v31, v61, v38, v31 op_sel:[1,0,0] op_sel_hi:[1,0,0]
	s_waitcnt vmcnt(0)
	v_cvt_scalef32_pk_f16_fp8 v58, v52, 1.0
	v_cvt_scalef32_pk_f16_fp8 v59, v52, 1.0 op_sel:[1,0,0]
	v_cvt_scalef32_pk_f16_fp8 v60, v53, 1.0
	v_cvt_scalef32_pk_f16_fp8 v61, v53, 1.0 op_sel:[1,0,0]
	v_fma_mix_f32 v16, v58, v39, v16 op_sel_hi:[1,0,0]
	v_fma_mix_f32 v17, v58, v39, v17 op_sel:[1,0,0] op_sel_hi:[1,0,0]
	v_fma_mix_f32 v18, v59, v39, v18 op_sel_hi:[1,0,0]
	v_fma_mix_f32 v19, v59, v39, v19 op_sel:[1,0,0] op_sel_hi:[1,0,0]
	v_fma_mix_f32 v20, v60, v39, v20 op_sel_hi:[1,0,0]
	v_fma_mix_f32 v21, v60, v39, v21 op_sel:[1,0,0] op_sel_hi:[1,0,0]
	v_fma_mix_f32 v22, v61, v39, v22 op_sel_hi:[1,0,0]
	v_fma_mix_f32 v23, v61, v39, v23 op_sel:[1,0,0] op_sel_hi:[1,0,0]
	v_cvt_scalef32_pk_f16_fp8 v58, v54, 1.0
	v_cvt_scalef32_pk_f16_fp8 v59, v54, 1.0 op_sel:[1,0,0]
	v_cvt_scalef32_pk_f16_fp8 v60, v55, 1.0
	v_cvt_scalef32_pk_f16_fp8 v61, v55, 1.0 op_sel:[1,0,0]
	v_fma_mix_f32 v24, v58, v39, v24 op_sel_hi:[1,0,0]
	v_fma_mix_f32 v25, v58, v39, v25 op_sel:[1,0,0] op_sel_hi:[1,0,0]
	v_fma_mix_f32 v26, v59, v39, v26 op_sel_hi:[1,0,0]
	v_fma_mix_f32 v27, v59, v39, v27 op_sel:[1,0,0] op_sel_hi:[1,0,0]
	v_fma_mix_f32 v28, v60, v39, v28 op_sel_hi:[1,0,0]
	v_fma_mix_f32 v29, v60, v39, v29 op_sel:[1,0,0] op_sel_hi:[1,0,0]
	v_fma_mix_f32 v30, v61, v39, v30 op_sel_hi:[1,0,0]
	v_fma_mix_f32 v31, v61, v39, v31 op_sel:[1,0,0] op_sel_hi:[1,0,0]
	s_sub_i32 s29, s29, 4
	s_branch .Lagg_B

.Lagg_epi:
	s_and_saveexec_b64 s[32:33], s[36:37]
	v_rcp_f32_e32 v57, v14
	ds_read_b128 v[32:35], v62 offset:0
	ds_read_b128 v[36:39], v62 offset:16
	ds_read_b128 v[40:43], v62 offset:512
	ds_read_b128 v[44:47], v62 offset:528
	ds_read_b128 v[48:51], v62 offset:1024
	ds_read_b128 v[52:55], v62 offset:1040
	s_waitcnt lgkmcnt(2)
	v_mul_f32_e32 v16, v16, v57
	v_mul_f32_e32 v17, v17, v57
	v_mul_f32_e32 v18, v18, v57
	v_mul_f32_e32 v19, v19, v57
	v_mul_f32_e32 v20, v20, v57
	v_mul_f32_e32 v21, v21, v57
	v_mul_f32_e32 v22, v22, v57
	v_mul_f32_e32 v23, v23, v57
	v_fma_f32 v16, v16, v32, v40
	v_fma_f32 v17, v17, v33, v41
	v_fma_f32 v18, v18, v34, v42
	v_fma_f32 v19, v19, v35, v43
	v_fma_f32 v20, v20, v36, v44
	v_fma_f32 v21, v21, v37, v45
	v_fma_f32 v22, v22, v38, v46
	v_fma_f32 v23, v23, v39, v47
	ds_read_b128 v[32:35], v62 offset:1536
	ds_read_b128 v[36:39], v62 offset:1552
	v_mul_f32_e32 v59, 0x3fb8aa3b, v16
	v_mul_f32_e32 v60, 0x3fb8aa3b, v17
	v_mul_f32_e32 v61, 0x3fb8aa3b, v18
	v_mul_f32_e32 v67, 0x3fb8aa3b, v19
	v_exp_f32_e32 v59, v59
	v_exp_f32_e32 v60, v60
	v_exp_f32_e32 v61, v61
	v_exp_f32_e32 v67, v67
	v_add_f32_e32 v59, -1.0, v59
	v_add_f32_e32 v60, -1.0, v60
	v_add_f32_e32 v61, -1.0, v61
	v_add_f32_e32 v67, -1.0, v67
	v_med3_f32 v16, v16, v59, 0
	v_med3_f32 v17, v17, v60, 0
	v_med3_f32 v18, v18, v61, 0
	v_med3_f32 v19, v19, v67, 0
	v_cvt_f16_f32_e32 v59, v16
	v_cvt_f16_f32_e32 v60, v17
	v_cvt_f16_f32_e32 v61, v18
	v_cvt_f16_f32_e32 v67, v19
	ds_write_b16 v3, v59
	ds_write_b16 v3, v60 offset:128
	ds_write_b16 v3, v61 offset:256
	ds_write_b16 v3, v67 offset:384
	v_mul_f32_e32 v59, 0x3fb8aa3b, v20
	v_mul_f32_e32 v60, 0x3fb8aa3b, v21
	v_mul_f32_e32 v61, 0x3fb8aa3b, v22
	v_mul_f32_e32 v67, 0x3fb8aa3b, v23
	v_exp_f32_e32 v59, v59
	v_exp_f32_e32 v60, v60
	v_exp_f32_e32 v61, v61
	v_exp_f32_e32 v67, v67
	v_add_f32_e32 v59, -1.0, v59
	v_add_f32_e32 v60, -1.0, v60
	v_add_f32_e32 v61, -1.0, v61
	v_add_f32_e32 v67, -1.0, v67
	v_med3_f32 v20, v20, v59, 0
	v_med3_f32 v21, v21, v60, 0
	v_med3_f32 v22, v22, v61, 0
	v_med3_f32 v23, v23, v67, 0
	v_cvt_f16_f32_e32 v59, v20
	v_cvt_f16_f32_e32 v60, v21
	v_cvt_f16_f32_e32 v61, v22
	v_cvt_f16_f32_e32 v67, v23
	ds_write_b16 v3, v59 offset:512
	ds_write_b16 v3, v60 offset:640
	ds_write_b16 v3, v61 offset:768
	ds_write_b16 v3, v67 offset:896
	s_waitcnt lgkmcnt(0)
	v_mul_f32_e32 v56, v16, v48
	v_mul_f32_e32 v58, v16, v32
	v_fmac_f32_e32 v56, v17, v49
	v_fmac_f32_e32 v58, v17, v33
	v_fmac_f32_e32 v56, v18, v50
	v_fmac_f32_e32 v58, v18, v34
	v_fmac_f32_e32 v56, v19, v51
	v_fmac_f32_e32 v58, v19, v35
	v_fmac_f32_e32 v56, v20, v52
	v_fmac_f32_e32 v58, v20, v36
	v_fmac_f32_e32 v56, v21, v53
	v_fmac_f32_e32 v58, v21, v37
	v_fmac_f32_e32 v56, v22, v54
	v_fmac_f32_e32 v58, v22, v38
	v_fmac_f32_e32 v56, v23, v55
	v_fmac_f32_e32 v58, v23, v39
	ds_read_b128 v[32:35], v62 offset:32
	ds_read_b128 v[36:39], v62 offset:48
	ds_read_b128 v[40:43], v62 offset:544
	ds_read_b128 v[44:47], v62 offset:560
	ds_read_b128 v[48:51], v62 offset:1056
	ds_read_b128 v[52:55], v62 offset:1072
	s_waitcnt lgkmcnt(2)
	v_mul_f32_e32 v24, v24, v57
	v_mul_f32_e32 v25, v25, v57
	v_mul_f32_e32 v26, v26, v57
	v_mul_f32_e32 v27, v27, v57
	v_mul_f32_e32 v28, v28, v57
	v_mul_f32_e32 v29, v29, v57
	v_mul_f32_e32 v30, v30, v57
	v_mul_f32_e32 v31, v31, v57
	v_fma_f32 v24, v24, v32, v40
	v_fma_f32 v25, v25, v33, v41
	v_fma_f32 v26, v26, v34, v42
	v_fma_f32 v27, v27, v35, v43
	v_fma_f32 v28, v28, v36, v44
	v_fma_f32 v29, v29, v37, v45
	v_fma_f32 v30, v30, v38, v46
	v_fma_f32 v31, v31, v39, v47
	ds_read_b128 v[32:35], v62 offset:1568
	ds_read_b128 v[36:39], v62 offset:1584
	v_mul_f32_e32 v59, 0x3fb8aa3b, v24
	v_mul_f32_e32 v60, 0x3fb8aa3b, v25
	v_mul_f32_e32 v61, 0x3fb8aa3b, v26
	v_mul_f32_e32 v67, 0x3fb8aa3b, v27
	v_exp_f32_e32 v59, v59
	v_exp_f32_e32 v60, v60
	v_exp_f32_e32 v61, v61
	v_exp_f32_e32 v67, v67
	v_add_f32_e32 v59, -1.0, v59
	v_add_f32_e32 v60, -1.0, v60
	v_add_f32_e32 v61, -1.0, v61
	v_add_f32_e32 v67, -1.0, v67
	v_med3_f32 v24, v24, v59, 0
	v_med3_f32 v25, v25, v60, 0
	v_med3_f32 v26, v26, v61, 0
	v_med3_f32 v27, v27, v67, 0
	v_cvt_f16_f32_e32 v59, v24
	v_cvt_f16_f32_e32 v60, v25
	v_cvt_f16_f32_e32 v61, v26
	v_cvt_f16_f32_e32 v67, v27
	ds_write_b16 v3, v59 offset:1024
	ds_write_b16 v3, v60 offset:1152
	ds_write_b16 v3, v61 offset:1280
	ds_write_b16 v3, v67 offset:1408
	v_mul_f32_e32 v59, 0x3fb8aa3b, v28
	v_mul_f32_e32 v60, 0x3fb8aa3b, v29
	v_mul_f32_e32 v61, 0x3fb8aa3b, v30
	v_mul_f32_e32 v67, 0x3fb8aa3b, v31
	v_exp_f32_e32 v59, v59
	v_exp_f32_e32 v60, v60
	v_exp_f32_e32 v61, v61
	v_exp_f32_e32 v67, v67
	v_add_f32_e32 v59, -1.0, v59
	v_add_f32_e32 v60, -1.0, v60
	v_add_f32_e32 v61, -1.0, v61
	v_add_f32_e32 v67, -1.0, v67
	v_med3_f32 v28, v28, v59, 0
	v_med3_f32 v29, v29, v60, 0
	v_med3_f32 v30, v30, v61, 0
	v_med3_f32 v31, v31, v67, 0
	v_cvt_f16_f32_e32 v59, v28
	v_cvt_f16_f32_e32 v60, v29
	v_cvt_f16_f32_e32 v61, v30
	v_cvt_f16_f32_e32 v67, v31
	ds_write_b16 v3, v59 offset:1536
	ds_write_b16 v3, v60 offset:1664
	ds_write_b16 v3, v61 offset:1792
	ds_write_b16 v3, v67 offset:1920
	s_waitcnt lgkmcnt(0)
	v_fmac_f32_e32 v56, v24, v48
	v_fmac_f32_e32 v58, v24, v32
	v_fmac_f32_e32 v56, v25, v49
	v_fmac_f32_e32 v58, v25, v33
	v_fmac_f32_e32 v56, v26, v50
	v_fmac_f32_e32 v58, v26, v34
	v_fmac_f32_e32 v56, v27, v51
	v_fmac_f32_e32 v58, v27, v35
	v_fmac_f32_e32 v56, v28, v52
	v_fmac_f32_e32 v58, v28, v36
	v_fmac_f32_e32 v56, v29, v53
	v_fmac_f32_e32 v58, v29, v37
	v_fmac_f32_e32 v56, v30, v54
	v_fmac_f32_e32 v58, v30, v38
	v_fmac_f32_e32 v56, v31, v55
	v_fmac_f32_e32 v58, v31, v39
	s_nop 1
	v_add_f32_dpp v56, v56, v56 quad_perm:[1,0,3,2] row_mask:0xf bank_mask:0xf
	v_add_f32_dpp v58, v58, v58 quad_perm:[1,0,3,2] row_mask:0xf bank_mask:0xf
	s_nop 0
	v_add_f32_dpp v56, v56, v56 quad_perm:[2,3,0,1] row_mask:0xf bank_mask:0xf
	v_add_f32_dpp v58, v58, v58 quad_perm:[2,3,0,1] row_mask:0xf bank_mask:0xf
	s_nop 0
	ds_swizzle_b32 v59, v56 offset:swizzle(SWAP,4)
	ds_swizzle_b32 v60, v58 offset:swizzle(SWAP,4)
	s_waitcnt lgkmcnt(0)
	v_add_f32_e32 v56, v56, v59
	v_add_f32_e32 v58, v58, v60
	s_and_b64 exec, exec, s[34:35]
	global_store_dword v4, v56, s[20:21]
	global_store_dword v4, v58, s[22:23]
	s_mov_b64 exec, s[32:33]
	s_waitcnt lgkmcnt(0)
	s_barrier
	ds_read_b128 v[32:35], v63
	ds_read_b128 v[36:39], v63 offset:128
	s_lshl_b32 s27, s2, 2
	s_add_i32 s27, s27, s25
	s_lshl_b32 s27, s27, 11
	v_and_b32_e32 v40, 63, v0
	v_lshlrev_b32_e32 v40, 5, v40
	v_add_u32_e32 v40, s27, v40
	s_waitcnt lgkmcnt(0)
	global_store_dwordx4 v40, v[32:35], s[18:19]
	global_store_dwordx4 v40, v[36:39], s[18:19] offset:16
	s_endpgm
